# back-edge rotation: in all 8 GEMM K-loops the loop counter / pointer bump / exit test now run before the loop-back barrier (where the wave parks anyway) instead of after its release
# baseline (speedup 1.0000x reference)
.Lcj2_253:
	s_setprio 0
	s_barrier
	v_add_u32_e32 v133, 0x18000, v131
	ds_read_b128 v[136:139], v133
	ds_read_b128 v[140:143], v133 offset:1024
	ds_read_b128 v[144:147], v133 offset:2048
	ds_read_b128 v[148:151], v133 offset:3072
	v_add_u32_e32 v133, 0x1c000, v131
	ds_read_b128 v[152:155], v133
	ds_read_b128 v[156:159], v133 offset:1024
	ds_read_b128 v[160:163], v133 offset:2048
	ds_read_b128 v[164:167], v133 offset:3072
	s_add_u32 s66, s66, 0x40000
	s_addc_u32 s67, s67, 0
	s_mov_b32 m0, s46
	ds_read_b128 v[168:171], v135 offset:32768
	ds_read_b128 v[172:175], v135 offset:33792
	ds_read_b128 v[176:179], v135 offset:34816
	ds_read_b128 v[180:183], v135 offset:35840
	ds_read_b128 v[184:187], v135 offset:36864
	ds_read_b128 v[188:191], v135 offset:37888
	ds_read_b128 v[196:199], v135 offset:38912
	ds_read_b128 v[200:203], v135 offset:39936
	global_load_lds_dwordx4 v194, s[66:67]
	s_mov_b32 m0, s47
	s_nop 0
	global_load_lds_dwordx4 v132, s[66:67]
	s_waitcnt vmcnt(8)
	s_waitcnt lgkmcnt(0)
	s_barrier
	s_setprio 1
	s_waitcnt lgkmcnt(0)
	v_mfma_f32_16x16x32_bf16 v[126:129], v[136:139], v[168:171], v[126:129]
	v_mfma_f32_16x16x32_bf16 v[122:125], v[144:147], v[168:171], v[122:125]
	v_mfma_f32_16x16x32_bf16 v[114:117], v[136:139], v[176:179], v[114:117]
	v_mfma_f32_16x16x32_bf16 v[110:113], v[144:147], v[176:179], v[110:113]
	v_mfma_f32_16x16x32_bf16 v[94:97], v[136:139], v[184:187], v[94:97]
	v_mfma_f32_16x16x32_bf16 v[90:93], v[144:147], v[184:187], v[90:93]
	v_mfma_f32_16x16x32_bf16 v[78:81], v[136:139], v[196:199], v[78:81]
	v_mfma_f32_16x16x32_bf16 v[74:77], v[144:147], v[196:199], v[74:77]
	v_mfma_f32_16x16x32_bf16 v[126:129], v[140:143], v[172:175], v[126:129]
	v_mfma_f32_16x16x32_bf16 v[122:125], v[148:151], v[172:175], v[122:125]
	v_mfma_f32_16x16x32_bf16 v[114:117], v[140:143], v[180:183], v[114:117]
	v_mfma_f32_16x16x32_bf16 v[110:113], v[148:151], v[180:183], v[110:113]
	v_mfma_f32_16x16x32_bf16 v[94:97], v[140:143], v[188:191], v[94:97]
	v_mfma_f32_16x16x32_bf16 v[90:93], v[148:151], v[188:191], v[90:93]
	v_mfma_f32_16x16x32_bf16 v[78:81], v[140:143], v[200:203], v[78:81]
	v_mfma_f32_16x16x32_bf16 v[74:77], v[148:151], v[200:203], v[74:77]
	s_setprio 0
	s_setprio 1
	v_mfma_f32_16x16x32_bf16 v[106:109], v[152:155], v[168:171], v[106:109]
	v_mfma_f32_16x16x32_bf16 v[118:121], v[160:163], v[168:171], v[118:121]
	v_mfma_f32_16x16x32_bf16 v[102:105], v[152:155], v[176:179], v[102:105]
	v_mfma_f32_16x16x32_bf16 v[98:101], v[160:163], v[176:179], v[98:101]
	v_mfma_f32_16x16x32_bf16 v[86:89], v[152:155], v[184:187], v[86:89]
	v_mfma_f32_16x16x32_bf16 v[82:85], v[160:163], v[184:187], v[82:85]
	v_mfma_f32_16x16x32_bf16 v[70:73], v[152:155], v[196:199], v[70:73]
	v_mfma_f32_16x16x32_bf16 v[66:69], v[160:163], v[196:199], v[66:69]
	v_mfma_f32_16x16x32_bf16 v[106:109], v[156:159], v[172:175], v[106:109]
	v_mfma_f32_16x16x32_bf16 v[118:121], v[164:167], v[172:175], v[118:121]
	v_mfma_f32_16x16x32_bf16 v[102:105], v[156:159], v[180:183], v[102:105]
	v_mfma_f32_16x16x32_bf16 v[98:101], v[164:167], v[180:183], v[98:101]
	v_mfma_f32_16x16x32_bf16 v[86:89], v[156:159], v[188:191], v[86:89]
	v_mfma_f32_16x16x32_bf16 v[82:85], v[164:167], v[188:191], v[82:85]
	v_mfma_f32_16x16x32_bf16 v[70:73], v[156:159], v[200:203], v[70:73]
	v_mfma_f32_16x16x32_bf16 v[66:69], v[164:167], v[200:203], v[66:69]
	s_setprio 0
	s_barrier
	s_or_b32 s62, s62, 1
	s_lshl_b64 s[66:67], s[62:63], 7
	s_add_u32 s68, s4, s66
	s_mov_b32 m0, s48
	s_addc_u32 s69, s5, s67
	ds_read_b128 v[168:171], v135 offset:49152
	ds_read_b128 v[172:175], v135 offset:50176
	ds_read_b128 v[176:179], v135 offset:51200
	ds_read_b128 v[180:183], v135 offset:52224
	ds_read_b128 v[184:187], v135 offset:53248
	ds_read_b128 v[188:191], v135 offset:54272
	ds_read_b128 v[196:199], v135 offset:55296
	ds_read_b128 v[200:203], v135 offset:56320
	global_load_lds_dwordx4 v130, s[68:69]
	s_mov_b32 m0, s49
	s_nop 0
	global_load_lds_dwordx4 v134, s[68:69]
	s_add_u32 s68, s72, s66
	s_addc_u32 s69, s73, s67
	s_mov_b32 m0, s52
	s_add_u32 s66, s0, s66
	global_load_lds_dwordx4 v130, s[68:69]
	s_mov_b32 m0, s53
	s_addc_u32 s67, s1, s67
	global_load_lds_dwordx4 v134, s[68:69]
	s_mov_b32 m0, s50
	s_nop 0
	global_load_lds_dwordx4 v194, s[66:67]
	s_mov_b32 m0, s51
	s_nop 0
	global_load_lds_dwordx4 v132, s[66:67]
	s_waitcnt vmcnt(8)
	s_waitcnt lgkmcnt(0)
	s_barrier
	s_setprio 1
	s_waitcnt lgkmcnt(0)
	v_mfma_f32_16x16x32_bf16 v[62:65], v[136:139], v[168:171], v[62:65]
	v_mfma_f32_16x16x32_bf16 v[58:61], v[144:147], v[168:171], v[58:61]
	v_mfma_f32_16x16x32_bf16 v[46:49], v[136:139], v[176:179], v[46:49]
	v_mfma_f32_16x16x32_bf16 v[42:45], v[144:147], v[176:179], v[42:45]
	v_mfma_f32_16x16x32_bf16 v[30:33], v[136:139], v[184:187], v[30:33]
	v_mfma_f32_16x16x32_bf16 v[26:29], v[144:147], v[184:187], v[26:29]
	v_mfma_f32_16x16x32_bf16 v[14:17], v[136:139], v[196:199], v[14:17]
	v_mfma_f32_16x16x32_bf16 v[10:13], v[144:147], v[196:199], v[10:13]
	v_mfma_f32_16x16x32_bf16 v[62:65], v[140:143], v[172:175], v[62:65]
	v_mfma_f32_16x16x32_bf16 v[58:61], v[148:151], v[172:175], v[58:61]
	v_mfma_f32_16x16x32_bf16 v[46:49], v[140:143], v[180:183], v[46:49]
	v_mfma_f32_16x16x32_bf16 v[42:45], v[148:151], v[180:183], v[42:45]
	v_mfma_f32_16x16x32_bf16 v[30:33], v[140:143], v[188:191], v[30:33]
	v_mfma_f32_16x16x32_bf16 v[26:29], v[148:151], v[188:191], v[26:29]
	v_mfma_f32_16x16x32_bf16 v[14:17], v[140:143], v[200:203], v[14:17]
	v_mfma_f32_16x16x32_bf16 v[10:13], v[148:151], v[200:203], v[10:13]
	s_setprio 0
	s_setprio 1
	v_mfma_f32_16x16x32_bf16 v[54:57], v[152:155], v[168:171], v[54:57]
	v_mfma_f32_16x16x32_bf16 v[50:53], v[160:163], v[168:171], v[50:53]
	v_mfma_f32_16x16x32_bf16 v[38:41], v[152:155], v[176:179], v[38:41]
	v_mfma_f32_16x16x32_bf16 v[34:37], v[160:163], v[176:179], v[34:37]
	v_mfma_f32_16x16x32_bf16 v[22:25], v[152:155], v[184:187], v[22:25]
	v_mfma_f32_16x16x32_bf16 v[18:21], v[160:163], v[184:187], v[18:21]
	v_mfma_f32_16x16x32_bf16 v[6:9], v[152:155], v[196:199], v[6:9]
	v_mfma_f32_16x16x32_bf16 v[2:5], v[160:163], v[196:199], v[2:5]
	v_mfma_f32_16x16x32_bf16 v[54:57], v[156:159], v[172:175], v[54:57]
	v_mfma_f32_16x16x32_bf16 v[50:53], v[164:167], v[172:175], v[50:53]
	v_mfma_f32_16x16x32_bf16 v[38:41], v[156:159], v[180:183], v[38:41]
	v_mfma_f32_16x16x32_bf16 v[34:37], v[164:167], v[180:183], v[34:37]
	v_mfma_f32_16x16x32_bf16 v[22:25], v[156:159], v[188:191], v[22:25]
	v_mfma_f32_16x16x32_bf16 v[18:21], v[164:167], v[188:191], v[18:21]
	v_mfma_f32_16x16x32_bf16 v[6:9], v[156:159], v[200:203], v[6:9]
	v_mfma_f32_16x16x32_bf16 v[2:5], v[164:167], v[200:203], v[2:5]
	s_setprio 0
	s_add_i32 s62, s61, 2
	s_add_u32 s26, s26, 0x100
	s_addc_u32 s27, s27, 0
	s_cmp_ge_i32 s61, s25
	s_mov_b32 s61, s62
	s_barrier
	s_cbranch_scc0 .LBB0_253
	s_branch .Lcsk_253

.Lcj2_287:
	s_setprio 0
	s_barrier
	v_add_u32_e32 v142, 0x18000, v165
	v_add_u32_e32 v158, 0x1c000, v165
	ds_read_b128 v[130:133], v142
	ds_read_b128 v[134:137], v142 offset:1024
	ds_read_b128 v[138:141], v142 offset:2048
	ds_read_b128 v[142:145], v142 offset:3072
	ds_read_b128 v[146:149], v158
	ds_read_b128 v[150:153], v158 offset:1024
	ds_read_b128 v[154:157], v158 offset:2048
	ds_read_b128 v[158:161], v158 offset:3072
	s_add_u32 s58, s58, 0x40000
	s_addc_u32 s59, s59, 0
	s_mov_b32 m0, s43
	v_lshl_add_u64 v[204:205], s[58:59], 0, v[194:195]
	ds_read_b128 v[174:177], v167 offset:32768
	ds_read_b128 v[178:181], v167 offset:33792
	ds_read_b128 v[182:185], v167 offset:34816
	ds_read_b128 v[186:189], v167 offset:35840
	ds_read_b128 v[190:193], v167 offset:36864
	ds_read_b128 v[196:199], v167 offset:37888
	ds_read_b128 v[200:203], v167 offset:38912
	ds_read_b128 v[216:219], v167 offset:39936
	global_load_lds_dwordx4 v[204:205], off
	v_lshl_add_u64 v[204:205], s[58:59], 0, v[162:163]
	s_mov_b32 m0, s44
	s_nop 0
	global_load_lds_dwordx4 v[204:205], off
	s_waitcnt vmcnt(8)
	s_waitcnt lgkmcnt(0)
	s_barrier
	s_setprio 1
	s_waitcnt lgkmcnt(0)
	v_mfma_f32_16x16x32_bf16 v[126:129], v[130:133], v[174:177], v[126:129]
	v_mfma_f32_16x16x32_bf16 v[122:125], v[138:141], v[174:177], v[122:125]
	v_mfma_f32_16x16x32_bf16 v[110:113], v[130:133], v[182:185], v[110:113]
	v_mfma_f32_16x16x32_bf16 v[106:109], v[138:141], v[182:185], v[106:109]
	v_mfma_f32_16x16x32_bf16 v[94:97], v[130:133], v[190:193], v[94:97]
	v_mfma_f32_16x16x32_bf16 v[90:93], v[138:141], v[190:193], v[90:93]
	v_mfma_f32_16x16x32_bf16 v[78:81], v[130:133], v[200:203], v[78:81]
	v_mfma_f32_16x16x32_bf16 v[74:77], v[138:141], v[200:203], v[74:77]
	v_mfma_f32_16x16x32_bf16 v[126:129], v[134:137], v[178:181], v[126:129]
	v_mfma_f32_16x16x32_bf16 v[122:125], v[142:145], v[178:181], v[122:125]
	v_mfma_f32_16x16x32_bf16 v[110:113], v[134:137], v[186:189], v[110:113]
	v_mfma_f32_16x16x32_bf16 v[106:109], v[142:145], v[186:189], v[106:109]
	v_mfma_f32_16x16x32_bf16 v[94:97], v[134:137], v[196:199], v[94:97]
	v_mfma_f32_16x16x32_bf16 v[90:93], v[142:145], v[196:199], v[90:93]
	v_mfma_f32_16x16x32_bf16 v[78:81], v[134:137], v[216:219], v[78:81]
	v_mfma_f32_16x16x32_bf16 v[74:77], v[142:145], v[216:219], v[74:77]
	s_setprio 0
	s_setprio 1
	v_mfma_f32_16x16x32_bf16 v[118:121], v[146:149], v[174:177], v[118:121]
	v_mfma_f32_16x16x32_bf16 v[114:117], v[154:157], v[174:177], v[114:117]
	v_mfma_f32_16x16x32_bf16 v[102:105], v[146:149], v[182:185], v[102:105]
	v_mfma_f32_16x16x32_bf16 v[98:101], v[154:157], v[182:185], v[98:101]
	v_mfma_f32_16x16x32_bf16 v[86:89], v[146:149], v[190:193], v[86:89]
	v_mfma_f32_16x16x32_bf16 v[82:85], v[154:157], v[190:193], v[82:85]
	v_mfma_f32_16x16x32_bf16 v[70:73], v[146:149], v[200:203], v[70:73]
	v_mfma_f32_16x16x32_bf16 v[66:69], v[154:157], v[200:203], v[66:69]
	v_mfma_f32_16x16x32_bf16 v[118:121], v[150:153], v[178:181], v[118:121]
	v_mfma_f32_16x16x32_bf16 v[114:117], v[158:161], v[178:181], v[114:117]
	v_mfma_f32_16x16x32_bf16 v[102:105], v[150:153], v[186:189], v[102:105]
	v_mfma_f32_16x16x32_bf16 v[98:101], v[158:161], v[186:189], v[98:101]
	v_mfma_f32_16x16x32_bf16 v[86:89], v[150:153], v[196:199], v[86:89]
	v_mfma_f32_16x16x32_bf16 v[82:85], v[158:161], v[196:199], v[82:85]
	v_mfma_f32_16x16x32_bf16 v[70:73], v[150:153], v[216:219], v[70:73]
	v_mfma_f32_16x16x32_bf16 v[66:69], v[158:161], v[216:219], v[66:69]
	s_setprio 0
	s_barrier
	s_add_u32 s57, s26, 0x80
	s_addc_u32 s58, s27, 0
	s_add_u32 s26, s18, s57
	s_mov_b32 m0, s46
	s_addc_u32 s27, s19, s58
	ds_read_b128 v[174:177], v167 offset:49152
	ds_read_b128 v[178:181], v167 offset:50176
	ds_read_b128 v[182:185], v167 offset:51200
	ds_read_b128 v[186:189], v167 offset:52224
	ds_read_b128 v[190:193], v167 offset:53248
	ds_read_b128 v[196:199], v167 offset:54272
	ds_read_b128 v[200:203], v167 offset:55296
	ds_read_b128 v[216:219], v167 offset:56320
	global_load_lds_dwordx4 v164, s[26:27]
	s_mov_b32 m0, s47
	s_nop 0
	global_load_lds_dwordx4 v168, s[26:27]
	s_mov_b32 m0, s50
	s_nop 0
	global_load_lds_dwordx4 v166, s[26:27]
	s_mov_b32 m0, s51
	s_nop 0
	global_load_lds_dwordx4 v170, s[26:27]
	s_add_u32 s26, s10, s57
	s_addc_u32 s27, s11, s58
	v_lshl_add_u64 v[204:205], s[26:27], 0, v[194:195]
	s_mov_b32 m0, s48
	s_nop 0
	global_load_lds_dwordx4 v[204:205], off
	v_lshl_add_u64 v[204:205], s[26:27], 0, v[162:163]
	s_mov_b32 m0, s49
	s_nop 0
	global_load_lds_dwordx4 v[204:205], off
	s_waitcnt vmcnt(8)
	s_waitcnt lgkmcnt(0)
	s_barrier
	s_setprio 1
	s_waitcnt lgkmcnt(0)
	v_mfma_f32_16x16x32_bf16 v[62:65], v[130:133], v[174:177], v[62:65]
	v_mfma_f32_16x16x32_bf16 v[58:61], v[138:141], v[174:177], v[58:61]
	v_mfma_f32_16x16x32_bf16 v[46:49], v[130:133], v[182:185], v[46:49]
	v_mfma_f32_16x16x32_bf16 v[42:45], v[138:141], v[182:185], v[42:45]
	v_mfma_f32_16x16x32_bf16 v[30:33], v[130:133], v[190:193], v[30:33]
	v_mfma_f32_16x16x32_bf16 v[26:29], v[138:141], v[190:193], v[26:29]
	v_mfma_f32_16x16x32_bf16 v[14:17], v[130:133], v[200:203], v[14:17]
	v_mfma_f32_16x16x32_bf16 v[10:13], v[138:141], v[200:203], v[10:13]
	v_mfma_f32_16x16x32_bf16 v[62:65], v[134:137], v[178:181], v[62:65]
	v_mfma_f32_16x16x32_bf16 v[58:61], v[142:145], v[178:181], v[58:61]
	v_mfma_f32_16x16x32_bf16 v[46:49], v[134:137], v[186:189], v[46:49]
	v_mfma_f32_16x16x32_bf16 v[42:45], v[142:145], v[186:189], v[42:45]
	v_mfma_f32_16x16x32_bf16 v[30:33], v[134:137], v[196:199], v[30:33]
	v_mfma_f32_16x16x32_bf16 v[26:29], v[142:145], v[196:199], v[26:29]
	v_mfma_f32_16x16x32_bf16 v[14:17], v[134:137], v[216:219], v[14:17]
	v_mfma_f32_16x16x32_bf16 v[10:13], v[142:145], v[216:219], v[10:13]
	s_setprio 0
	s_setprio 1
	v_mfma_f32_16x16x32_bf16 v[54:57], v[146:149], v[174:177], v[54:57]
	v_mfma_f32_16x16x32_bf16 v[50:53], v[154:157], v[174:177], v[50:53]
	v_mfma_f32_16x16x32_bf16 v[38:41], v[146:149], v[182:185], v[38:41]
	v_mfma_f32_16x16x32_bf16 v[34:37], v[154:157], v[182:185], v[34:37]
	v_mfma_f32_16x16x32_bf16 v[22:25], v[146:149], v[190:193], v[22:25]
	v_mfma_f32_16x16x32_bf16 v[18:21], v[154:157], v[190:193], v[18:21]
	v_mfma_f32_16x16x32_bf16 v[6:9], v[146:149], v[200:203], v[6:9]
	v_mfma_f32_16x16x32_bf16 v[2:5], v[154:157], v[200:203], v[2:5]
	v_mfma_f32_16x16x32_bf16 v[54:57], v[150:153], v[178:181], v[54:57]
	v_mfma_f32_16x16x32_bf16 v[50:53], v[158:161], v[178:181], v[50:53]
	v_mfma_f32_16x16x32_bf16 v[38:41], v[150:153], v[186:189], v[38:41]
	v_mfma_f32_16x16x32_bf16 v[34:37], v[158:161], v[186:189], v[34:37]
	v_mfma_f32_16x16x32_bf16 v[22:25], v[150:153], v[196:199], v[22:25]
	v_mfma_f32_16x16x32_bf16 v[18:21], v[158:161], v[196:199], v[18:21]
	v_mfma_f32_16x16x32_bf16 v[6:9], v[150:153], v[216:219], v[6:9]
	v_mfma_f32_16x16x32_bf16 v[2:5], v[158:161], v[216:219], v[2:5]
	s_setprio 0
	s_add_i32 s26, s56, 2
	s_add_u32 s24, s24, 0x100
	s_addc_u32 s25, s25, 0
	s_cmp_ge_i32 s56, s55
	s_barrier
	s_cbranch_scc1 .LBB0_292
	s_mov_b32 s56, s26
	s_branch .LBB0_287

.Lcj2_374:
	s_setprio 0
	s_barrier
	v_add_u32_e32 v142, 0x18000, v217
	v_add_u32_e32 v158, 0x1c000, v217
	ds_read_b128 v[130:133], v142
	ds_read_b128 v[134:137], v142 offset:1024
	ds_read_b128 v[138:141], v142 offset:2048
	ds_read_b128 v[142:145], v142 offset:3072
	ds_read_b128 v[146:149], v158
	ds_read_b128 v[150:153], v158 offset:1024
	ds_read_b128 v[154:157], v158 offset:2048
	ds_read_b128 v[158:161], v158 offset:3072
	s_add_u32 s58, s58, 0x8000
	s_addc_u32 s59, s59, 0
	s_mov_b32 m0, s43
	ds_read_b128 v[162:165], v221 offset:32768
	ds_read_b128 v[166:169], v221 offset:33792
	ds_read_b128 v[170:173], v221 offset:34816
	ds_read_b128 v[174:177], v221 offset:35840
	ds_read_b128 v[178:181], v221 offset:36864
	ds_read_b128 v[182:185], v221 offset:37888
	ds_read_b128 v[186:189], v221 offset:38912
	ds_read_b128 v[190:193], v221 offset:39936
	global_load_lds_dwordx4 v194, s[58:59]
	s_mov_b32 m0, s44
	s_nop 0
	global_load_lds_dwordx4 v218, s[58:59]
	s_waitcnt vmcnt(8)
	s_waitcnt lgkmcnt(0)
	s_barrier
	s_setprio 1
	s_waitcnt lgkmcnt(0)
	v_mfma_f32_16x16x32_bf16 v[126:129], v[130:133], v[162:165], v[126:129]
	v_mfma_f32_16x16x32_bf16 v[122:125], v[138:141], v[162:165], v[122:125]
	v_mfma_f32_16x16x32_bf16 v[94:97], v[130:133], v[170:173], v[94:97]
	v_mfma_f32_16x16x32_bf16 v[86:89], v[138:141], v[170:173], v[86:89]
	v_mfma_f32_16x16x32_bf16 v[62:65], v[130:133], v[178:181], v[62:65]
	v_mfma_f32_16x16x32_bf16 v[54:57], v[138:141], v[178:181], v[54:57]
	v_mfma_f32_16x16x32_bf16 v[30:33], v[130:133], v[186:189], v[30:33]
	v_mfma_f32_16x16x32_bf16 v[22:25], v[138:141], v[186:189], v[22:25]
	v_mfma_f32_16x16x32_bf16 v[126:129], v[134:137], v[166:169], v[126:129]
	v_mfma_f32_16x16x32_bf16 v[122:125], v[142:145], v[166:169], v[122:125]
	v_mfma_f32_16x16x32_bf16 v[94:97], v[134:137], v[174:177], v[94:97]
	v_mfma_f32_16x16x32_bf16 v[86:89], v[142:145], v[174:177], v[86:89]
	v_mfma_f32_16x16x32_bf16 v[62:65], v[134:137], v[182:185], v[62:65]
	v_mfma_f32_16x16x32_bf16 v[54:57], v[142:145], v[182:185], v[54:57]
	v_mfma_f32_16x16x32_bf16 v[30:33], v[134:137], v[190:193], v[30:33]
	v_mfma_f32_16x16x32_bf16 v[22:25], v[142:145], v[190:193], v[22:25]
	s_setprio 0
	s_setprio 1
	v_mfma_f32_16x16x32_bf16 v[110:113], v[146:149], v[162:165], v[110:113]
	v_mfma_f32_16x16x32_bf16 v[102:105], v[154:157], v[162:165], v[102:105]
	v_mfma_f32_16x16x32_bf16 v[78:81], v[146:149], v[170:173], v[78:81]
	v_mfma_f32_16x16x32_bf16 v[70:73], v[154:157], v[170:173], v[70:73]
	v_mfma_f32_16x16x32_bf16 v[46:49], v[146:149], v[178:181], v[46:49]
	v_mfma_f32_16x16x32_bf16 v[38:41], v[154:157], v[178:181], v[38:41]
	v_mfma_f32_16x16x32_bf16 v[14:17], v[146:149], v[186:189], v[14:17]
	v_mfma_f32_16x16x32_bf16 v[6:9], v[154:157], v[186:189], v[6:9]
	v_mfma_f32_16x16x32_bf16 v[110:113], v[150:153], v[166:169], v[110:113]
	v_mfma_f32_16x16x32_bf16 v[102:105], v[158:161], v[166:169], v[102:105]
	v_mfma_f32_16x16x32_bf16 v[78:81], v[150:153], v[174:177], v[78:81]
	v_mfma_f32_16x16x32_bf16 v[70:73], v[158:161], v[174:177], v[70:73]
	v_mfma_f32_16x16x32_bf16 v[46:49], v[150:153], v[182:185], v[46:49]
	v_mfma_f32_16x16x32_bf16 v[38:41], v[158:161], v[182:185], v[38:41]
	v_mfma_f32_16x16x32_bf16 v[14:17], v[150:153], v[190:193], v[14:17]
	v_mfma_f32_16x16x32_bf16 v[6:9], v[158:161], v[190:193], v[6:9]
	s_setprio 0
	s_barrier
	s_or_b32 s62, s62, 1
	s_lshl_b64 s[58:59], s[62:63], 7
	s_add_u32 s60, s8, s58
	s_mov_b32 m0, s45
	s_addc_u32 s61, s9, s59
	ds_read_b128 v[162:165], v221 offset:49152
	ds_read_b128 v[166:169], v221 offset:50176
	ds_read_b128 v[170:173], v221 offset:51200
	ds_read_b128 v[174:177], v221 offset:52224
	ds_read_b128 v[178:181], v221 offset:53248
	ds_read_b128 v[182:185], v221 offset:54272
	ds_read_b128 v[186:189], v221 offset:55296
	ds_read_b128 v[190:193], v221 offset:56320
	global_load_lds_dwordx4 v216, s[60:61]
	s_mov_b32 m0, s46
	s_nop 0
	global_load_lds_dwordx4 v220, s[60:61]
	s_add_u32 s60, s57, s58
	s_addc_u32 s61, s66, s59
	s_mov_b32 m0, s49
	s_add_u32 s58, s20, s58
	global_load_lds_dwordx4 v216, s[60:61]
	s_mov_b32 m0, s50
	s_addc_u32 s59, s21, s59
	global_load_lds_dwordx4 v220, s[60:61]
	s_mov_b32 m0, s47
	s_nop 0
	global_load_lds_dwordx4 v194, s[58:59]
	s_mov_b32 m0, s48
	s_nop 0
	global_load_lds_dwordx4 v218, s[58:59]
	s_waitcnt vmcnt(8)
	s_waitcnt lgkmcnt(0)
	s_barrier
	s_setprio 1
	s_waitcnt lgkmcnt(0)
	v_mfma_f32_16x16x32_bf16 v[118:121], v[130:133], v[162:165], v[118:121]
	v_mfma_f32_16x16x32_bf16 v[114:117], v[138:141], v[162:165], v[114:117]
	v_mfma_f32_16x16x32_bf16 v[90:93], v[130:133], v[170:173], v[90:93]
	v_mfma_f32_16x16x32_bf16 v[82:85], v[138:141], v[170:173], v[82:85]
	v_mfma_f32_16x16x32_bf16 v[58:61], v[130:133], v[178:181], v[58:61]
	v_mfma_f32_16x16x32_bf16 v[50:53], v[138:141], v[178:181], v[50:53]
	v_mfma_f32_16x16x32_bf16 v[26:29], v[130:133], v[186:189], v[26:29]
	v_mfma_f32_16x16x32_bf16 v[18:21], v[138:141], v[186:189], v[18:21]
	v_mfma_f32_16x16x32_bf16 v[118:121], v[134:137], v[166:169], v[118:121]
	v_mfma_f32_16x16x32_bf16 v[114:117], v[142:145], v[166:169], v[114:117]
	v_mfma_f32_16x16x32_bf16 v[90:93], v[134:137], v[174:177], v[90:93]
	v_mfma_f32_16x16x32_bf16 v[82:85], v[142:145], v[174:177], v[82:85]
	v_mfma_f32_16x16x32_bf16 v[58:61], v[134:137], v[182:185], v[58:61]
	v_mfma_f32_16x16x32_bf16 v[50:53], v[142:145], v[182:185], v[50:53]
	v_mfma_f32_16x16x32_bf16 v[26:29], v[134:137], v[190:193], v[26:29]
	v_mfma_f32_16x16x32_bf16 v[18:21], v[142:145], v[190:193], v[18:21]
	s_setprio 0
	s_setprio 1
	v_mfma_f32_16x16x32_bf16 v[106:109], v[146:149], v[162:165], v[106:109]
	v_mfma_f32_16x16x32_bf16 v[98:101], v[154:157], v[162:165], v[98:101]
	v_mfma_f32_16x16x32_bf16 v[74:77], v[146:149], v[170:173], v[74:77]
	v_mfma_f32_16x16x32_bf16 v[66:69], v[154:157], v[170:173], v[66:69]
	v_mfma_f32_16x16x32_bf16 v[42:45], v[146:149], v[178:181], v[42:45]
	v_mfma_f32_16x16x32_bf16 v[34:37], v[154:157], v[178:181], v[34:37]
	v_mfma_f32_16x16x32_bf16 v[10:13], v[146:149], v[186:189], v[10:13]
	v_mfma_f32_16x16x32_bf16 v[2:5], v[154:157], v[186:189], v[2:5]
	v_mfma_f32_16x16x32_bf16 v[106:109], v[150:153], v[166:169], v[106:109]
	v_mfma_f32_16x16x32_bf16 v[98:101], v[158:161], v[166:169], v[98:101]
	v_mfma_f32_16x16x32_bf16 v[74:77], v[150:153], v[174:177], v[74:77]
	v_mfma_f32_16x16x32_bf16 v[66:69], v[158:161], v[174:177], v[66:69]
	v_mfma_f32_16x16x32_bf16 v[42:45], v[150:153], v[182:185], v[42:45]
	v_mfma_f32_16x16x32_bf16 v[34:37], v[158:161], v[182:185], v[34:37]
	v_mfma_f32_16x16x32_bf16 v[10:13], v[150:153], v[190:193], v[10:13]
	v_mfma_f32_16x16x32_bf16 v[2:5], v[158:161], v[190:193], v[2:5]
	s_setprio 0
	s_add_i32 s57, s56, 2
	s_add_u32 s24, s24, 0x100
	s_addc_u32 s25, s25, 0
	s_cmp_ge_i32 s56, s54
	s_mov_b32 s56, s57
	s_barrier
	s_cbranch_scc0 .LBB0_374
	s_branch .Lcsk_374

.Lcj2_492:
	s_setprio 0
	s_barrier
	v_add_u32_e32 v142, 0x18000, v165
	v_add_u32_e32 v158, 0x1c000, v165
	ds_read_b128 v[130:133], v142
	ds_read_b128 v[134:137], v142 offset:1024
	ds_read_b128 v[138:141], v142 offset:2048
	ds_read_b128 v[142:145], v142 offset:3072
	ds_read_b128 v[146:149], v158
	ds_read_b128 v[150:153], v158 offset:1024
	ds_read_b128 v[154:157], v158 offset:2048
	ds_read_b128 v[158:161], v158 offset:3072
	s_add_u32 s56, s56, 0x10000
	s_addc_u32 s57, s57, 0
	s_mov_b32 m0, s40
	v_lshl_add_u64 v[204:205], s[56:57], 0, v[194:195]
	ds_read_b128 v[174:177], v167 offset:32768
	ds_read_b128 v[178:181], v167 offset:33792
	ds_read_b128 v[182:185], v167 offset:34816
	ds_read_b128 v[186:189], v167 offset:35840
	ds_read_b128 v[190:193], v167 offset:36864
	ds_read_b128 v[196:199], v167 offset:37888
	ds_read_b128 v[200:203], v167 offset:38912
	ds_read_b128 v[216:219], v167 offset:39936
	global_load_lds_dwordx4 v[204:205], off
	v_lshl_add_u64 v[204:205], s[56:57], 0, v[162:163]
	s_mov_b32 m0, s41
	s_nop 0
	global_load_lds_dwordx4 v[204:205], off
	s_waitcnt vmcnt(8)
	s_waitcnt lgkmcnt(0)
	s_barrier
	s_setprio 1
	s_waitcnt lgkmcnt(0)
	v_mfma_f32_16x16x32_bf16 v[126:129], v[130:133], v[174:177], v[126:129]
	v_mfma_f32_16x16x32_bf16 v[122:125], v[138:141], v[174:177], v[122:125]
	v_mfma_f32_16x16x32_bf16 v[110:113], v[130:133], v[182:185], v[110:113]
	v_mfma_f32_16x16x32_bf16 v[106:109], v[138:141], v[182:185], v[106:109]
	v_mfma_f32_16x16x32_bf16 v[94:97], v[130:133], v[190:193], v[94:97]
	v_mfma_f32_16x16x32_bf16 v[90:93], v[138:141], v[190:193], v[90:93]
	v_mfma_f32_16x16x32_bf16 v[78:81], v[130:133], v[200:203], v[78:81]
	v_mfma_f32_16x16x32_bf16 v[74:77], v[138:141], v[200:203], v[74:77]
	v_mfma_f32_16x16x32_bf16 v[126:129], v[134:137], v[178:181], v[126:129]
	v_mfma_f32_16x16x32_bf16 v[122:125], v[142:145], v[178:181], v[122:125]
	v_mfma_f32_16x16x32_bf16 v[110:113], v[134:137], v[186:189], v[110:113]
	v_mfma_f32_16x16x32_bf16 v[106:109], v[142:145], v[186:189], v[106:109]
	v_mfma_f32_16x16x32_bf16 v[94:97], v[134:137], v[196:199], v[94:97]
	v_mfma_f32_16x16x32_bf16 v[90:93], v[142:145], v[196:199], v[90:93]
	v_mfma_f32_16x16x32_bf16 v[78:81], v[134:137], v[216:219], v[78:81]
	v_mfma_f32_16x16x32_bf16 v[74:77], v[142:145], v[216:219], v[74:77]
	s_setprio 0
	s_setprio 1
	v_mfma_f32_16x16x32_bf16 v[118:121], v[146:149], v[174:177], v[118:121]
	v_mfma_f32_16x16x32_bf16 v[114:117], v[154:157], v[174:177], v[114:117]
	v_mfma_f32_16x16x32_bf16 v[102:105], v[146:149], v[182:185], v[102:105]
	v_mfma_f32_16x16x32_bf16 v[98:101], v[154:157], v[182:185], v[98:101]
	v_mfma_f32_16x16x32_bf16 v[86:89], v[146:149], v[190:193], v[86:89]
	v_mfma_f32_16x16x32_bf16 v[82:85], v[154:157], v[190:193], v[82:85]
	v_mfma_f32_16x16x32_bf16 v[70:73], v[146:149], v[200:203], v[70:73]
	v_mfma_f32_16x16x32_bf16 v[66:69], v[154:157], v[200:203], v[66:69]
	v_mfma_f32_16x16x32_bf16 v[118:121], v[150:153], v[178:181], v[118:121]
	v_mfma_f32_16x16x32_bf16 v[114:117], v[158:161], v[178:181], v[114:117]
	v_mfma_f32_16x16x32_bf16 v[102:105], v[150:153], v[186:189], v[102:105]
	v_mfma_f32_16x16x32_bf16 v[98:101], v[158:161], v[186:189], v[98:101]
	v_mfma_f32_16x16x32_bf16 v[86:89], v[150:153], v[196:199], v[86:89]
	v_mfma_f32_16x16x32_bf16 v[82:85], v[158:161], v[196:199], v[82:85]
	v_mfma_f32_16x16x32_bf16 v[70:73], v[150:153], v[216:219], v[70:73]
	v_mfma_f32_16x16x32_bf16 v[66:69], v[158:161], v[216:219], v[66:69]
	s_setprio 0
	s_barrier
	s_add_u32 s56, s24, 0x80
	s_addc_u32 s57, s25, 0
	s_add_u32 s24, s14, s56
	s_mov_b32 m0, s43
	s_addc_u32 s25, s15, s57
	ds_read_b128 v[174:177], v167 offset:49152
	ds_read_b128 v[178:181], v167 offset:50176
	ds_read_b128 v[182:185], v167 offset:51200
	ds_read_b128 v[186:189], v167 offset:52224
	ds_read_b128 v[190:193], v167 offset:53248
	ds_read_b128 v[196:199], v167 offset:54272
	ds_read_b128 v[200:203], v167 offset:55296
	ds_read_b128 v[216:219], v167 offset:56320
	global_load_lds_dwordx4 v164, s[24:25]
	s_mov_b32 m0, s44
	s_nop 0
	global_load_lds_dwordx4 v168, s[24:25]
	s_mov_b32 m0, s47
	s_nop 0
	global_load_lds_dwordx4 v166, s[24:25]
	s_mov_b32 m0, s48
	s_nop 0
	global_load_lds_dwordx4 v170, s[24:25]
	s_add_u32 s24, s16, s56
	s_addc_u32 s25, s17, s57
	v_lshl_add_u64 v[204:205], s[24:25], 0, v[194:195]
	s_mov_b32 m0, s45
	s_nop 0
	global_load_lds_dwordx4 v[204:205], off
	v_lshl_add_u64 v[204:205], s[24:25], 0, v[162:163]
	s_mov_b32 m0, s46
	s_nop 0
	global_load_lds_dwordx4 v[204:205], off
	s_waitcnt vmcnt(8)
	s_waitcnt lgkmcnt(0)
	s_barrier
	s_setprio 1
	s_waitcnt lgkmcnt(0)
	v_mfma_f32_16x16x32_bf16 v[62:65], v[130:133], v[174:177], v[62:65]
	v_mfma_f32_16x16x32_bf16 v[58:61], v[138:141], v[174:177], v[58:61]
	v_mfma_f32_16x16x32_bf16 v[46:49], v[130:133], v[182:185], v[46:49]
	v_mfma_f32_16x16x32_bf16 v[42:45], v[138:141], v[182:185], v[42:45]
	v_mfma_f32_16x16x32_bf16 v[30:33], v[130:133], v[190:193], v[30:33]
	v_mfma_f32_16x16x32_bf16 v[26:29], v[138:141], v[190:193], v[26:29]
	v_mfma_f32_16x16x32_bf16 v[14:17], v[130:133], v[200:203], v[14:17]
	v_mfma_f32_16x16x32_bf16 v[10:13], v[138:141], v[200:203], v[10:13]
	v_mfma_f32_16x16x32_bf16 v[62:65], v[134:137], v[178:181], v[62:65]
	v_mfma_f32_16x16x32_bf16 v[58:61], v[142:145], v[178:181], v[58:61]
	v_mfma_f32_16x16x32_bf16 v[46:49], v[134:137], v[186:189], v[46:49]
	v_mfma_f32_16x16x32_bf16 v[42:45], v[142:145], v[186:189], v[42:45]
	v_mfma_f32_16x16x32_bf16 v[30:33], v[134:137], v[196:199], v[30:33]
	v_mfma_f32_16x16x32_bf16 v[26:29], v[142:145], v[196:199], v[26:29]
	v_mfma_f32_16x16x32_bf16 v[14:17], v[134:137], v[216:219], v[14:17]
	v_mfma_f32_16x16x32_bf16 v[10:13], v[142:145], v[216:219], v[10:13]
	s_setprio 0
	s_setprio 1
	v_mfma_f32_16x16x32_bf16 v[54:57], v[146:149], v[174:177], v[54:57]
	v_mfma_f32_16x16x32_bf16 v[50:53], v[154:157], v[174:177], v[50:53]
	v_mfma_f32_16x16x32_bf16 v[38:41], v[146:149], v[182:185], v[38:41]
	v_mfma_f32_16x16x32_bf16 v[34:37], v[154:157], v[182:185], v[34:37]
	v_mfma_f32_16x16x32_bf16 v[22:25], v[146:149], v[190:193], v[22:25]
	v_mfma_f32_16x16x32_bf16 v[18:21], v[154:157], v[190:193], v[18:21]
	v_mfma_f32_16x16x32_bf16 v[6:9], v[146:149], v[200:203], v[6:9]
	v_mfma_f32_16x16x32_bf16 v[2:5], v[154:157], v[200:203], v[2:5]
	v_mfma_f32_16x16x32_bf16 v[54:57], v[150:153], v[178:181], v[54:57]
	v_mfma_f32_16x16x32_bf16 v[50:53], v[158:161], v[178:181], v[50:53]
	v_mfma_f32_16x16x32_bf16 v[38:41], v[150:153], v[186:189], v[38:41]
	v_mfma_f32_16x16x32_bf16 v[34:37], v[158:161], v[186:189], v[34:37]
	v_mfma_f32_16x16x32_bf16 v[22:25], v[150:153], v[196:199], v[22:25]
	v_mfma_f32_16x16x32_bf16 v[18:21], v[158:161], v[196:199], v[18:21]
	v_mfma_f32_16x16x32_bf16 v[6:9], v[150:153], v[216:219], v[6:9]
	v_mfma_f32_16x16x32_bf16 v[2:5], v[158:161], v[216:219], v[2:5]
	s_setprio 0
	s_add_i32 s24, s55, 2
	s_add_u32 s22, s22, 0x100
	s_addc_u32 s23, s23, 0
	s_cmp_ge_i32 s55, s52
	s_barrier
	s_cbranch_scc1 .LBB0_497
	s_mov_b32 s55, s24
	s_branch .LBB0_492

.Lcj2_579:
	s_setprio 0
	s_barrier
	v_add_u32_e32 v142, 0x18000, v191
	v_add_u32_e32 v158, 0x1c000, v191
	ds_read_b128 v[130:133], v142
	ds_read_b128 v[134:137], v142 offset:1024
	ds_read_b128 v[138:141], v142 offset:2048
	ds_read_b128 v[142:145], v142 offset:3072
	ds_read_b128 v[146:149], v158
	ds_read_b128 v[150:153], v158 offset:1024
	ds_read_b128 v[154:157], v158 offset:2048
	ds_read_b128 v[158:161], v158 offset:3072
	s_add_u32 s68, s68, 0x60000
	s_addc_u32 s69, s69, 0
	s_mov_b32 m0, s42
	ds_read_b128 v[162:165], v217 offset:32768
	ds_read_b128 v[166:169], v217 offset:33792
	ds_read_b128 v[170:173], v217 offset:34816
	ds_read_b128 v[174:177], v217 offset:35840
	ds_read_b128 v[178:181], v217 offset:36864
	ds_read_b128 v[182:185], v217 offset:37888
	ds_read_b128 v[186:189], v217 offset:38912
	ds_read_b128 v[196:199], v217 offset:39936
	global_load_lds_dwordx4 v194, s[68:69]
	s_mov_b32 m0, s43
	s_nop 0
	global_load_lds_dwordx4 v192, s[68:69]
	s_waitcnt vmcnt(8)
	s_waitcnt lgkmcnt(0)
	s_barrier
	s_setprio 1
	s_waitcnt lgkmcnt(0)
	v_mfma_f32_16x16x32_bf16 v[122:125], v[130:133], v[162:165], v[122:125]
	v_mfma_f32_16x16x32_bf16 v[126:129], v[138:141], v[162:165], v[126:129]
	v_mfma_f32_16x16x32_bf16 v[110:113], v[130:133], v[170:173], v[110:113]
	v_mfma_f32_16x16x32_bf16 v[106:109], v[138:141], v[170:173], v[106:109]
	v_mfma_f32_16x16x32_bf16 v[94:97], v[130:133], v[178:181], v[94:97]
	v_mfma_f32_16x16x32_bf16 v[90:93], v[138:141], v[178:181], v[90:93]
	v_mfma_f32_16x16x32_bf16 v[78:81], v[130:133], v[186:189], v[78:81]
	v_mfma_f32_16x16x32_bf16 v[74:77], v[138:141], v[186:189], v[74:77]
	v_mfma_f32_16x16x32_bf16 v[122:125], v[134:137], v[166:169], v[122:125]
	v_mfma_f32_16x16x32_bf16 v[126:129], v[142:145], v[166:169], v[126:129]
	v_mfma_f32_16x16x32_bf16 v[110:113], v[134:137], v[174:177], v[110:113]
	v_mfma_f32_16x16x32_bf16 v[106:109], v[142:145], v[174:177], v[106:109]
	v_mfma_f32_16x16x32_bf16 v[94:97], v[134:137], v[182:185], v[94:97]
	v_mfma_f32_16x16x32_bf16 v[90:93], v[142:145], v[182:185], v[90:93]
	v_mfma_f32_16x16x32_bf16 v[78:81], v[134:137], v[196:199], v[78:81]
	v_mfma_f32_16x16x32_bf16 v[74:77], v[142:145], v[196:199], v[74:77]
	s_setprio 0
	s_setprio 1
	v_mfma_f32_16x16x32_bf16 v[118:121], v[146:149], v[162:165], v[118:121]
	v_mfma_f32_16x16x32_bf16 v[114:117], v[154:157], v[162:165], v[114:117]
	v_mfma_f32_16x16x32_bf16 v[102:105], v[146:149], v[170:173], v[102:105]
	v_mfma_f32_16x16x32_bf16 v[98:101], v[154:157], v[170:173], v[98:101]
	v_mfma_f32_16x16x32_bf16 v[86:89], v[146:149], v[178:181], v[86:89]
	v_mfma_f32_16x16x32_bf16 v[82:85], v[154:157], v[178:181], v[82:85]
	v_mfma_f32_16x16x32_bf16 v[70:73], v[146:149], v[186:189], v[70:73]
	v_mfma_f32_16x16x32_bf16 v[66:69], v[154:157], v[186:189], v[66:69]
	v_mfma_f32_16x16x32_bf16 v[118:121], v[150:153], v[166:169], v[118:121]
	v_mfma_f32_16x16x32_bf16 v[114:117], v[158:161], v[166:169], v[114:117]
	v_mfma_f32_16x16x32_bf16 v[102:105], v[150:153], v[174:177], v[102:105]
	v_mfma_f32_16x16x32_bf16 v[98:101], v[158:161], v[174:177], v[98:101]
	v_mfma_f32_16x16x32_bf16 v[86:89], v[150:153], v[182:185], v[86:89]
	v_mfma_f32_16x16x32_bf16 v[82:85], v[158:161], v[182:185], v[82:85]
	v_mfma_f32_16x16x32_bf16 v[70:73], v[150:153], v[196:199], v[70:73]
	v_mfma_f32_16x16x32_bf16 v[66:69], v[158:161], v[196:199], v[66:69]
	s_setprio 0
	s_barrier
	s_or_b32 s62, s62, 1
	s_lshl_b64 s[68:69], s[62:63], 7
	s_add_u32 s72, s6, s68
	s_mov_b32 m0, s46
	s_addc_u32 s73, s7, s69
	ds_read_b128 v[162:165], v217 offset:49152
	ds_read_b128 v[166:169], v217 offset:50176
	ds_read_b128 v[170:173], v217 offset:51200
	ds_read_b128 v[174:177], v217 offset:52224
	ds_read_b128 v[178:181], v217 offset:53248
	ds_read_b128 v[182:185], v217 offset:54272
	ds_read_b128 v[186:189], v217 offset:55296
	ds_read_b128 v[196:199], v217 offset:56320
	global_load_lds_dwordx4 v190, s[72:73]
	s_mov_b32 m0, s47
	s_nop 0
	global_load_lds_dwordx4 v216, s[72:73]
	s_add_u32 s72, s61, s68
	s_addc_u32 s73, s67, s69
	s_mov_b32 m0, s50
	s_add_u32 s68, s0, s68
	global_load_lds_dwordx4 v190, s[72:73]
	s_mov_b32 m0, s51
	s_addc_u32 s69, s1, s69
	global_load_lds_dwordx4 v216, s[72:73]
	s_mov_b32 m0, s48
	s_nop 0
	global_load_lds_dwordx4 v194, s[68:69]
	s_mov_b32 m0, s49
	s_nop 0
	global_load_lds_dwordx4 v192, s[68:69]
	s_waitcnt vmcnt(8)
	s_waitcnt lgkmcnt(0)
	s_barrier
	s_setprio 1
	s_waitcnt lgkmcnt(0)
	v_mfma_f32_16x16x32_bf16 v[62:65], v[130:133], v[162:165], v[62:65]
	v_mfma_f32_16x16x32_bf16 v[58:61], v[138:141], v[162:165], v[58:61]
	v_mfma_f32_16x16x32_bf16 v[46:49], v[130:133], v[170:173], v[46:49]
	v_mfma_f32_16x16x32_bf16 v[42:45], v[138:141], v[170:173], v[42:45]
	v_mfma_f32_16x16x32_bf16 v[30:33], v[130:133], v[178:181], v[30:33]
	v_mfma_f32_16x16x32_bf16 v[26:29], v[138:141], v[178:181], v[26:29]
	v_mfma_f32_16x16x32_bf16 v[14:17], v[130:133], v[186:189], v[14:17]
	v_mfma_f32_16x16x32_bf16 v[10:13], v[138:141], v[186:189], v[10:13]
	v_mfma_f32_16x16x32_bf16 v[62:65], v[134:137], v[166:169], v[62:65]
	v_mfma_f32_16x16x32_bf16 v[58:61], v[142:145], v[166:169], v[58:61]
	v_mfma_f32_16x16x32_bf16 v[46:49], v[134:137], v[174:177], v[46:49]
	v_mfma_f32_16x16x32_bf16 v[42:45], v[142:145], v[174:177], v[42:45]
	v_mfma_f32_16x16x32_bf16 v[30:33], v[134:137], v[182:185], v[30:33]
	v_mfma_f32_16x16x32_bf16 v[26:29], v[142:145], v[182:185], v[26:29]
	v_mfma_f32_16x16x32_bf16 v[14:17], v[134:137], v[196:199], v[14:17]
	v_mfma_f32_16x16x32_bf16 v[10:13], v[142:145], v[196:199], v[10:13]
	s_setprio 0
	s_setprio 1
	v_mfma_f32_16x16x32_bf16 v[54:57], v[146:149], v[162:165], v[54:57]
	v_mfma_f32_16x16x32_bf16 v[50:53], v[154:157], v[162:165], v[50:53]
	v_mfma_f32_16x16x32_bf16 v[38:41], v[146:149], v[170:173], v[38:41]
	v_mfma_f32_16x16x32_bf16 v[34:37], v[154:157], v[170:173], v[34:37]
	v_mfma_f32_16x16x32_bf16 v[22:25], v[146:149], v[178:181], v[22:25]
	v_mfma_f32_16x16x32_bf16 v[18:21], v[154:157], v[178:181], v[18:21]
	v_mfma_f32_16x16x32_bf16 v[6:9], v[146:149], v[186:189], v[6:9]
	v_mfma_f32_16x16x32_bf16 v[2:5], v[154:157], v[186:189], v[2:5]
	v_mfma_f32_16x16x32_bf16 v[54:57], v[150:153], v[166:169], v[54:57]
	v_mfma_f32_16x16x32_bf16 v[50:53], v[158:161], v[166:169], v[50:53]
	v_mfma_f32_16x16x32_bf16 v[38:41], v[150:153], v[174:177], v[38:41]
	v_mfma_f32_16x16x32_bf16 v[34:37], v[158:161], v[174:177], v[34:37]
	v_mfma_f32_16x16x32_bf16 v[22:25], v[150:153], v[182:185], v[22:25]
	v_mfma_f32_16x16x32_bf16 v[18:21], v[158:161], v[182:185], v[18:21]
	v_mfma_f32_16x16x32_bf16 v[6:9], v[150:153], v[196:199], v[6:9]
	v_mfma_f32_16x16x32_bf16 v[2:5], v[158:161], v[196:199], v[2:5]
	s_setprio 0
	s_add_u32 s22, s22, 0x100
	s_addc_u32 s23, s23, 0
	s_cmp_ge_i32 s66, s58
	s_barrier
	s_cbranch_scc1 .LBB0_583
	s_mov_b32 s61, s66
	s_mov_b32 s73, 0x10000
	s_branch .LBB0_579

.Lcj2_662:
	s_setprio 0
	s_barrier
	v_add_u32_e32 v142, 0x18000, v191
	v_add_u32_e32 v158, 0x1c000, v191
	ds_read_b128 v[130:133], v142
	ds_read_b128 v[134:137], v142 offset:1024
	ds_read_b128 v[138:141], v142 offset:2048
	ds_read_b128 v[142:145], v142 offset:3072
	ds_read_b128 v[146:149], v158
	ds_read_b128 v[150:153], v158 offset:1024
	ds_read_b128 v[154:157], v158 offset:2048
	ds_read_b128 v[158:161], v158 offset:3072
	s_add_u32 s56, s56, 0x40000
	s_addc_u32 s57, s57, 0
	s_mov_b32 m0, s42
	ds_read_b128 v[162:165], v217 offset:32768
	ds_read_b128 v[166:169], v217 offset:33792
	ds_read_b128 v[170:173], v217 offset:34816
	ds_read_b128 v[174:177], v217 offset:35840
	ds_read_b128 v[178:181], v217 offset:36864
	ds_read_b128 v[182:185], v217 offset:37888
	ds_read_b128 v[186:189], v217 offset:38912
	ds_read_b128 v[196:199], v217 offset:39936
	global_load_lds_dwordx4 v194, s[56:57]
	s_mov_b32 m0, s43
	s_nop 0
	global_load_lds_dwordx4 v192, s[56:57]
	s_waitcnt vmcnt(8)
	s_waitcnt lgkmcnt(0)
	s_barrier
	s_setprio 1
	s_waitcnt lgkmcnt(0)
	v_mfma_f32_16x16x32_bf16 v[126:129], v[130:133], v[162:165], v[126:129]
	v_mfma_f32_16x16x32_bf16 v[122:125], v[138:141], v[162:165], v[122:125]
	v_mfma_f32_16x16x32_bf16 v[110:113], v[130:133], v[170:173], v[110:113]
	v_mfma_f32_16x16x32_bf16 v[106:109], v[138:141], v[170:173], v[106:109]
	v_mfma_f32_16x16x32_bf16 v[94:97], v[130:133], v[178:181], v[94:97]
	v_mfma_f32_16x16x32_bf16 v[90:93], v[138:141], v[178:181], v[90:93]
	v_mfma_f32_16x16x32_bf16 v[78:81], v[130:133], v[186:189], v[78:81]
	v_mfma_f32_16x16x32_bf16 v[74:77], v[138:141], v[186:189], v[74:77]
	v_mfma_f32_16x16x32_bf16 v[126:129], v[134:137], v[166:169], v[126:129]
	v_mfma_f32_16x16x32_bf16 v[122:125], v[142:145], v[166:169], v[122:125]
	v_mfma_f32_16x16x32_bf16 v[110:113], v[134:137], v[174:177], v[110:113]
	v_mfma_f32_16x16x32_bf16 v[106:109], v[142:145], v[174:177], v[106:109]
	v_mfma_f32_16x16x32_bf16 v[94:97], v[134:137], v[182:185], v[94:97]
	v_mfma_f32_16x16x32_bf16 v[90:93], v[142:145], v[182:185], v[90:93]
	v_mfma_f32_16x16x32_bf16 v[78:81], v[134:137], v[196:199], v[78:81]
	v_mfma_f32_16x16x32_bf16 v[74:77], v[142:145], v[196:199], v[74:77]
	s_setprio 0
	s_setprio 1
	v_mfma_f32_16x16x32_bf16 v[118:121], v[146:149], v[162:165], v[118:121]
	v_mfma_f32_16x16x32_bf16 v[114:117], v[154:157], v[162:165], v[114:117]
	v_mfma_f32_16x16x32_bf16 v[102:105], v[146:149], v[170:173], v[102:105]
	v_mfma_f32_16x16x32_bf16 v[98:101], v[154:157], v[170:173], v[98:101]
	v_mfma_f32_16x16x32_bf16 v[86:89], v[146:149], v[178:181], v[86:89]
	v_mfma_f32_16x16x32_bf16 v[82:85], v[154:157], v[178:181], v[82:85]
	v_mfma_f32_16x16x32_bf16 v[70:73], v[146:149], v[186:189], v[70:73]
	v_mfma_f32_16x16x32_bf16 v[66:69], v[154:157], v[186:189], v[66:69]
	v_mfma_f32_16x16x32_bf16 v[118:121], v[150:153], v[166:169], v[118:121]
	v_mfma_f32_16x16x32_bf16 v[114:117], v[158:161], v[166:169], v[114:117]
	v_mfma_f32_16x16x32_bf16 v[102:105], v[150:153], v[174:177], v[102:105]
	v_mfma_f32_16x16x32_bf16 v[98:101], v[158:161], v[174:177], v[98:101]
	v_mfma_f32_16x16x32_bf16 v[86:89], v[150:153], v[182:185], v[86:89]
	v_mfma_f32_16x16x32_bf16 v[82:85], v[158:161], v[182:185], v[82:85]
	v_mfma_f32_16x16x32_bf16 v[70:73], v[150:153], v[196:199], v[70:73]
	v_mfma_f32_16x16x32_bf16 v[66:69], v[158:161], v[196:199], v[66:69]
	s_setprio 0
	s_barrier
	s_or_b32 s62, s62, 1
	s_lshl_b64 s[56:57], s[62:63], 7
	s_add_u32 s58, s4, s56
	s_mov_b32 m0, s45
	s_addc_u32 s59, s5, s57
	ds_read_b128 v[162:165], v217 offset:49152
	ds_read_b128 v[166:169], v217 offset:50176
	ds_read_b128 v[170:173], v217 offset:51200
	ds_read_b128 v[174:177], v217 offset:52224
	ds_read_b128 v[178:181], v217 offset:53248
	ds_read_b128 v[182:185], v217 offset:54272
	ds_read_b128 v[186:189], v217 offset:55296
	ds_read_b128 v[196:199], v217 offset:56320
	global_load_lds_dwordx4 v190, s[58:59]
	s_mov_b32 m0, s46
	s_nop 0
	global_load_lds_dwordx4 v216, s[58:59]
	s_add_u32 s58, s60, s56
	s_addc_u32 s59, s61, s57
	s_mov_b32 m0, s49
	s_add_u32 s56, s0, s56
	global_load_lds_dwordx4 v190, s[58:59]
	s_mov_b32 m0, s50
	s_addc_u32 s57, s1, s57
	global_load_lds_dwordx4 v216, s[58:59]
	s_mov_b32 m0, s47
	s_nop 0
	global_load_lds_dwordx4 v194, s[56:57]
	s_mov_b32 m0, s48
	s_nop 0
	global_load_lds_dwordx4 v192, s[56:57]
	s_waitcnt vmcnt(8)
	s_waitcnt lgkmcnt(0)
	s_barrier
	s_setprio 1
	s_waitcnt lgkmcnt(0)
	v_mfma_f32_16x16x32_bf16 v[62:65], v[130:133], v[162:165], v[62:65]
	v_mfma_f32_16x16x32_bf16 v[58:61], v[138:141], v[162:165], v[58:61]
	v_mfma_f32_16x16x32_bf16 v[46:49], v[130:133], v[170:173], v[46:49]
	v_mfma_f32_16x16x32_bf16 v[42:45], v[138:141], v[170:173], v[42:45]
	v_mfma_f32_16x16x32_bf16 v[30:33], v[130:133], v[178:181], v[30:33]
	v_mfma_f32_16x16x32_bf16 v[26:29], v[138:141], v[178:181], v[26:29]
	v_mfma_f32_16x16x32_bf16 v[14:17], v[130:133], v[186:189], v[14:17]
	v_mfma_f32_16x16x32_bf16 v[10:13], v[138:141], v[186:189], v[10:13]
	v_mfma_f32_16x16x32_bf16 v[62:65], v[134:137], v[166:169], v[62:65]
	v_mfma_f32_16x16x32_bf16 v[58:61], v[142:145], v[166:169], v[58:61]
	v_mfma_f32_16x16x32_bf16 v[46:49], v[134:137], v[174:177], v[46:49]
	v_mfma_f32_16x16x32_bf16 v[42:45], v[142:145], v[174:177], v[42:45]
	v_mfma_f32_16x16x32_bf16 v[30:33], v[134:137], v[182:185], v[30:33]
	v_mfma_f32_16x16x32_bf16 v[26:29], v[142:145], v[182:185], v[26:29]
	v_mfma_f32_16x16x32_bf16 v[14:17], v[134:137], v[196:199], v[14:17]
	v_mfma_f32_16x16x32_bf16 v[10:13], v[142:145], v[196:199], v[10:13]
	s_setprio 0
	s_setprio 1
	v_mfma_f32_16x16x32_bf16 v[54:57], v[146:149], v[162:165], v[54:57]
	v_mfma_f32_16x16x32_bf16 v[50:53], v[154:157], v[162:165], v[50:53]
	v_mfma_f32_16x16x32_bf16 v[38:41], v[146:149], v[170:173], v[38:41]
	v_mfma_f32_16x16x32_bf16 v[34:37], v[154:157], v[170:173], v[34:37]
	v_mfma_f32_16x16x32_bf16 v[22:25], v[146:149], v[178:181], v[22:25]
	v_mfma_f32_16x16x32_bf16 v[18:21], v[154:157], v[178:181], v[18:21]
	v_mfma_f32_16x16x32_bf16 v[6:9], v[146:149], v[186:189], v[6:9]
	v_mfma_f32_16x16x32_bf16 v[2:5], v[154:157], v[186:189], v[2:5]
	v_mfma_f32_16x16x32_bf16 v[54:57], v[150:153], v[166:169], v[54:57]
	v_mfma_f32_16x16x32_bf16 v[50:53], v[158:161], v[166:169], v[50:53]
	v_mfma_f32_16x16x32_bf16 v[38:41], v[150:153], v[174:177], v[38:41]
	v_mfma_f32_16x16x32_bf16 v[34:37], v[158:161], v[174:177], v[34:37]
	v_mfma_f32_16x16x32_bf16 v[22:25], v[150:153], v[182:185], v[22:25]
	v_mfma_f32_16x16x32_bf16 v[18:21], v[158:161], v[182:185], v[18:21]
	v_mfma_f32_16x16x32_bf16 v[6:9], v[150:153], v[196:199], v[6:9]
	v_mfma_f32_16x16x32_bf16 v[2:5], v[158:161], v[196:199], v[2:5]
	s_setprio 0
	s_add_i32 s56, s55, 2
	s_add_u32 s22, s22, 0x100
	s_addc_u32 s23, s23, 0
	s_cmp_ge_i32 s55, s52
	s_mov_b32 s55, s56
	s_barrier
	s_cbranch_scc0 .LBB0_662
	s_branch .Lcsk_662

.Lcj2_961:
	s_setprio 0
	s_barrier
	v_add_u32_e32 v14, 0x18000, v167
	v_add_u32_e32 v30, 0x1c000, v167
	ds_read_b128 v[2:5], v14
	ds_read_b128 v[6:9], v14 offset:1024
	ds_read_b128 v[10:13], v14 offset:2048
	ds_read_b128 v[14:17], v14 offset:3072
	ds_read_b128 v[18:21], v30
	ds_read_b128 v[22:25], v30 offset:1024
	ds_read_b128 v[26:29], v30 offset:2048
	ds_read_b128 v[30:33], v30 offset:3072
	s_mov_b32 m0, s47
	v_lshl_add_u64 v[180:181], s[66:67], 0, v[194:195]
	ds_read_b128 v[34:37], v170 offset:32768
	ds_read_b128 v[38:41], v170 offset:33792
	ds_read_b128 v[42:45], v170 offset:34816
	ds_read_b128 v[46:49], v170 offset:35840
	ds_read_b128 v[50:53], v170 offset:36864
	ds_read_b128 v[54:57], v170 offset:37888
	ds_read_b128 v[58:61], v170 offset:38912
	ds_read_b128 v[62:65], v170 offset:39936
	global_load_lds_dwordx4 v[180:181], off
	v_lshl_add_u64 v[180:181], s[66:67], 0, v[168:169]
	s_mov_b32 m0, s48
	s_nop 0
	global_load_lds_dwordx4 v[180:181], off
	s_waitcnt vmcnt(8)
	s_waitcnt lgkmcnt(0)
	s_barrier
	s_setprio 1
	s_waitcnt lgkmcnt(0)
	v_mfma_f32_16x16x128_f8f6f4 v[146:149], v[2:9], v[34:41], v[146:149]
	v_mfma_f32_16x16x128_f8f6f4 v[158:161], v[10:17], v[34:41], v[158:161]
	v_mfma_f32_16x16x128_f8f6f4 v[142:145], v[2:9], v[42:49], v[142:145]
	v_mfma_f32_16x16x128_f8f6f4 v[138:141], v[10:17], v[42:49], v[138:141]
	v_mfma_f32_16x16x128_f8f6f4 v[126:129], v[2:9], v[50:57], v[126:129]
	v_mfma_f32_16x16x128_f8f6f4 v[122:125], v[10:17], v[50:57], v[122:125]
	v_mfma_f32_16x16x128_f8f6f4 v[110:113], v[2:9], v[58:65], v[110:113]
	v_mfma_f32_16x16x128_f8f6f4 v[106:109], v[10:17], v[58:65], v[106:109]
	s_setprio 0
	s_setprio 1
	v_mfma_f32_16x16x128_f8f6f4 v[154:157], v[18:25], v[34:41], v[154:157]
	v_mfma_f32_16x16x128_f8f6f4 v[150:153], v[26:33], v[34:41], v[150:153]
	v_mfma_f32_16x16x128_f8f6f4 v[134:137], v[18:25], v[42:49], v[134:137]
	v_mfma_f32_16x16x128_f8f6f4 v[130:133], v[26:33], v[42:49], v[130:133]
	v_mfma_f32_16x16x128_f8f6f4 v[118:121], v[18:25], v[50:57], v[118:121]
	v_mfma_f32_16x16x128_f8f6f4 v[114:117], v[26:33], v[50:57], v[114:117]
	v_mfma_f32_16x16x128_f8f6f4 v[102:105], v[18:25], v[58:65], v[102:105]
	v_mfma_f32_16x16x128_f8f6f4 v[98:101], v[26:33], v[58:65], v[98:101]
	s_setprio 0
	s_barrier
	s_add_u32 s61, s28, 0x80
	s_addc_u32 s62, s29, 0
	s_add_u32 s28, s12, s61
	s_mov_b32 m0, s49
	s_addc_u32 s29, s13, s62
	ds_read_b128 v[34:37], v170 offset:49152
	ds_read_b128 v[38:41], v170 offset:50176
	ds_read_b128 v[50:53], v170 offset:51200
	ds_read_b128 v[54:57], v170 offset:52224
	ds_read_b128 v[180:183], v170 offset:53248
	ds_read_b128 v[184:187], v170 offset:54272
	ds_read_b128 v[196:199], v170 offset:55296
	ds_read_b128 v[200:203], v170 offset:56320
	global_load_lds_dwordx4 v171, s[28:29]
	s_mov_b32 m0, s50
	s_nop 0
	global_load_lds_dwordx4 v162, s[28:29]
	s_add_u32 s28, s30, s61
	s_addc_u32 s29, s31, s62
	s_mov_b32 m0, s53
	s_nop 0
	global_load_lds_dwordx4 v171, s[28:29]
	s_mov_b32 m0, s54
	s_nop 0
	global_load_lds_dwordx4 v162, s[28:29]
	s_add_u32 s28, s20, s61
	s_addc_u32 s29, s21, s62
	s_mov_b32 m0, s51
	s_nop 0
	global_load_lds_dwordx4 v164, s[28:29]
	s_mov_b32 m0, s52
	s_nop 0
	global_load_lds_dwordx4 v166, s[28:29]
	s_waitcnt vmcnt(8)
	s_waitcnt lgkmcnt(0)
	s_barrier
	s_setprio 1
	s_waitcnt lgkmcnt(0)
	v_mfma_f32_16x16x128_f8f6f4 v[94:97], v[2:9], v[34:41], v[94:97]
	v_mfma_f32_16x16x128_f8f6f4 v[90:93], v[10:17], v[34:41], v[90:93]
	v_mfma_f32_16x16x128_f8f6f4 v[78:81], v[2:9], v[50:57], v[78:81]
	v_mfma_f32_16x16x128_f8f6f4 v[74:77], v[10:17], v[50:57], v[74:77]
	v_mfma_f32_16x16x128_f8f6f4 v[62:65], v[2:9], v[180:187], v[188:191]
	v_mfma_f32_16x16x128_f8f6f4 v[58:61], v[10:17], v[180:187], v[248:251]
	v_mfma_f32_16x16x128_f8f6f4 v[46:49], v[2:9], v[196:203], v[242:245]
	v_mfma_f32_16x16x128_f8f6f4 v[42:45], v[10:17], v[196:203], v[208:211]
	s_setprio 0
	s_setprio 1
	v_mfma_f32_16x16x128_f8f6f4 v[86:89], v[18:25], v[34:41], v[86:89]
	v_mfma_f32_16x16x128_f8f6f4 v[82:85], v[26:33], v[34:41], v[82:85]
	v_mfma_f32_16x16x128_f8f6f4 v[70:73], v[18:25], v[50:57], v[70:73]
	v_mfma_f32_16x16x128_f8f6f4 v[66:69], v[26:33], v[50:57], v[66:69]
	v_mfma_f32_16x16x128_f8f6f4 v[54:57], v[18:25], v[180:187], v[212:215]
	v_mfma_f32_16x16x128_f8f6f4 v[50:53], v[26:33], v[180:187], v[216:219]
	v_mfma_f32_16x16x128_f8f6f4 v[38:41], v[18:25], v[196:203], v[220:223]
	v_mfma_f32_16x16x128_f8f6f4 v[34:37], v[26:33], v[196:203], v[224:227]
	s_setprio 0
	s_add_i32 s28, s60, 2
	s_add_u32 s26, s26, 0x100
	s_addc_u32 s27, s27, 0
	s_cmp_ge_i32 s60, s19
	s_barrier
	s_cbranch_scc1 .LBB0_966
	s_mov_b32 s60, s28
	s_branch .LBB0_961

.Lcj2_1048:
	s_setprio 0
	s_barrier
	v_add_u32_e32 v10, 0x18000, v131
	s_nop 3
	ds_read_b128 v[2:5], v10
	ds_read_b128 v[6:9], v10 offset:1024
	ds_read_b128 v[18:21], v10 offset:2048
	ds_read_b128 v[22:25], v10 offset:3072
	v_add_u32_e32 v10, 0x1c000, v131
	ds_read_b128 v[136:139], v10
	ds_read_b128 v[140:143], v10 offset:1024
	ds_read_b128 v[144:147], v10 offset:2048
	ds_read_b128 v[148:151], v10 offset:3072
	s_add_u32 s58, s58, 0x58000
	s_addc_u32 s59, s59, 0
	s_mov_b32 m0, s41
	ds_read_b128 v[10:13], v135 offset:32768
	ds_read_b128 v[14:17], v135 offset:33792
	ds_read_b128 v[26:29], v135 offset:34816
	ds_read_b128 v[30:33], v135 offset:35840
	ds_read_b128 v[34:37], v135 offset:36864
	ds_read_b128 v[38:41], v135 offset:37888
	ds_read_b128 v[42:45], v135 offset:38912
	ds_read_b128 v[46:49], v135 offset:39936
	global_load_lds_dwordx4 v194, s[58:59]
	s_mov_b32 m0, s42
	s_nop 0
	global_load_lds_dwordx4 v132, s[58:59]
	s_waitcnt vmcnt(8)
	s_waitcnt lgkmcnt(0)
	s_barrier
	s_setprio 1
	s_waitcnt lgkmcnt(0)
	v_mfma_f32_16x16x128_f8f6f4 v[126:129], v[2:9], v[10:17], v[126:129]
	v_mfma_f32_16x16x128_f8f6f4 v[122:125], v[18:25], v[10:17], v[122:125]
	v_mfma_f32_16x16x128_f8f6f4 v[110:113], v[2:9], v[26:33], v[110:113]
	v_mfma_f32_16x16x128_f8f6f4 v[106:109], v[18:25], v[26:33], v[106:109]
	v_mfma_f32_16x16x128_f8f6f4 v[94:97], v[2:9], v[34:41], v[208:211]
	v_mfma_f32_16x16x128_f8f6f4 v[90:93], v[18:25], v[34:41], v[212:215]
	v_mfma_f32_16x16x128_f8f6f4 v[78:81], v[2:9], v[42:49], v[216:219]
	v_mfma_f32_16x16x128_f8f6f4 v[74:77], v[18:25], v[42:49], v[220:223]
	s_setprio 0
	s_setprio 1
	v_mfma_f32_16x16x128_f8f6f4 v[118:121], v[136:143], v[10:17], v[118:121]
	v_mfma_f32_16x16x128_f8f6f4 v[114:117], v[144:151], v[10:17], v[114:117]
	v_mfma_f32_16x16x128_f8f6f4 v[102:105], v[136:143], v[26:33], v[102:105]
	v_mfma_f32_16x16x128_f8f6f4 v[98:101], v[144:151], v[26:33], v[98:101]
	v_mfma_f32_16x16x128_f8f6f4 v[86:89], v[136:143], v[34:41], v[168:171]
	v_mfma_f32_16x16x128_f8f6f4 v[82:85], v[144:151], v[34:41], v[172:175]
	v_mfma_f32_16x16x128_f8f6f4 v[70:73], v[136:143], v[42:49], v[176:179]
	v_mfma_f32_16x16x128_f8f6f4 v[10:13], v[144:151], v[42:49], v[180:183]
	s_setprio 0
	s_barrier
	s_or_b32 s62, s62, 1
	s_lshl_b64 s[58:59], s[62:63], 7
	s_add_u32 s60, s6, s58
	s_mov_b32 m0, s43
	s_addc_u32 s61, s7, s59
	ds_read_b128 v[34:37], v135 offset:49152
	ds_read_b128 v[38:41], v135 offset:50176
	ds_read_b128 v[152:155], v135 offset:51200
	ds_read_b128 v[156:159], v135 offset:52224
	ds_read_b128 v[160:163], v135 offset:53248
	ds_read_b128 v[164:167], v135 offset:54272
	ds_read_b128 v[168:171], v135 offset:55296
	ds_read_b128 v[172:175], v135 offset:56320
	global_load_lds_dwordx4 v130, s[60:61]
	s_mov_b32 m0, s44
	s_add_u32 s22, s22, s58
	global_load_lds_dwordx4 v134, s[60:61]
	s_addc_u32 s23, s23, s59
	s_mov_b32 m0, s47
	s_nop 0
	global_load_lds_dwordx4 v130, s[22:23]
	s_mov_b32 m0, s48
	s_nop 0
	global_load_lds_dwordx4 v134, s[22:23]
	s_add_u32 s22, s0, s58
	s_addc_u32 s23, s1, s59
	s_mov_b32 m0, s45
	s_nop 0
	global_load_lds_dwordx4 v194, s[22:23]
	s_mov_b32 m0, s46
	s_nop 0
	global_load_lds_dwordx4 v132, s[22:23]
	s_waitcnt vmcnt(8)
	s_waitcnt lgkmcnt(0)
	s_barrier
	s_setprio 1
	s_waitcnt lgkmcnt(0)
	v_mfma_f32_16x16x128_f8f6f4 v[62:65], v[2:9], v[34:41], v[62:65]
	v_mfma_f32_16x16x128_f8f6f4 v[58:61], v[18:25], v[34:41], v[58:61]
	v_mfma_f32_16x16x128_f8f6f4 v[46:49], v[2:9], v[152:159], v[184:187]
	v_mfma_f32_16x16x128_f8f6f4 v[42:45], v[18:25], v[152:159], v[188:191]
	v_mfma_f32_16x16x128_f8f6f4 v[30:33], v[2:9], v[160:167], v[196:199]
	v_mfma_f32_16x16x128_f8f6f4 v[26:29], v[18:25], v[160:167], v[200:203]
	v_mfma_f32_16x16x128_f8f6f4 v[14:17], v[2:9], v[168:175], v[224:227]
	v_mfma_f32_16x16x128_f8f6f4 v[228:231], v[18:25], v[168:175], v[228:231]
	s_setprio 0
	s_setprio 1
	v_mfma_f32_16x16x128_f8f6f4 v[54:57], v[136:143], v[34:41], v[54:57]
	v_mfma_f32_16x16x128_f8f6f4 v[50:53], v[144:151], v[34:41], v[50:53]
	v_mfma_f32_16x16x128_f8f6f4 v[38:41], v[136:143], v[152:159], v[242:245]
	v_mfma_f32_16x16x128_f8f6f4 v[34:37], v[144:151], v[152:159], v[248:251]
	v_mfma_f32_16x16x128_f8f6f4 v[22:25], v[136:143], v[160:167], v[232:235]
	v_mfma_f32_16x16x128_f8f6f4 v[18:21], v[144:151], v[160:167], v[238:241]
	v_mfma_f32_16x16x128_f8f6f4 v[6:9], v[136:143], v[168:175], v[204:207]
	v_mfma_f32_16x16x128_f8f6f4 v[2:5], v[144:151], v[168:175], v[66:69]
	s_setprio 0
	s_add_i32 s22, s56, 2
	s_add_u32 s20, s20, 0x100
	s_addc_u32 s21, s21, 0
	s_cmp_ge_i32 s56, s55
	s_mov_b32 s56, s22
	s_barrier
	s_cbranch_scc0 .LBB0_1048
	s_branch .Lcsk_1048
